# k_fused: waves whose own key tile is masked-dead skip the K/V projection MFMAs (only G/Q projection)
# baseline (speedup 1.0000x reference)
_Z7k_fusedPKDF16_S0_S0_S0_PKfS2_S2_Pf:
	v_lshrrev_b32_e32 v222, 6, v0
	v_and_b32_e32 v1, 63, v0
	s_load_dwordx8 s[24:31], s[0:1], 0x8
	s_load_dwordx4 s[36:39], s[0:1], 0x28
	v_lshlrev_b32_e32 v4, 2, v222
	v_lshlrev_b32_e32 v5, 3, v1
	v_lshl_or_b32 v2, v222, 11, v5
	v_lshlrev_b32_e32 v224, 12, v222
	v_or_b32_e32 v6, 1, v4
	v_lshlrev_b32_e32 v223, 1, v2
	v_readfirstlane_b32 s3, v224
	v_lshl_or_b32 v2, v6, 9, v5
	v_lshlrev_b32_e32 v225, 10, v6
	v_mov_b32_e32 v211, 0
	s_mov_b32 m0, s3
	v_lshlrev_b32_e32 v210, 1, v2
	v_readfirstlane_b32 s3, v225
	s_waitcnt lgkmcnt(0)
	global_load_lds_dwordx4 v223, s[24:25]
	v_lshl_add_u64 v[2:3], s[24:25], 0, v[210:211]
	s_mov_b32 m0, s3
	v_or_b32_e32 v6, 2, v4
	global_load_lds_dwordx4 v[2:3], off
	v_lshl_or_b32 v2, v6, 9, v5
	v_lshlrev_b32_e32 v212, 1, v2
	v_mov_b32_e32 v213, v211
	v_lshl_add_u64 v[2:3], s[24:25], 0, v[212:213]
	v_lshlrev_b32_e32 v213, 10, v6
	v_or_b32_e32 v4, 3, v4
	v_readfirstlane_b32 s3, v213
	s_mov_b32 m0, s3
	v_mov_b32_e32 v215, v211
	global_load_lds_dwordx4 v[2:3], off
	v_lshl_or_b32 v2, v4, 9, v5
	v_lshlrev_b32_e32 v214, 1, v2
	v_lshl_add_u64 v[2:3], s[24:25], 0, v[214:215]
	v_lshlrev_b32_e32 v215, 10, v4
	s_nop 0
	v_readfirstlane_b32 s3, v215
	s_mov_b32 m0, s3
	s_movk_i32 s3, 0xff
	global_load_lds_dwordx4 v[2:3], off
	v_and_b32_e32 v2, 0x7f, v0
	v_lshlrev_b32_e32 v2, 2, v2
	global_load_dword v4, v2, s[36:37]
	global_load_dword v5, v2, s[38:39]
	s_lshl_b32 s3, s2, 8
	s_load_dwordx2 s[4:5], s[0:1], 0x0
	v_and_b32_e32 v6, 0xff, v0
	v_or_b32_e32 v6, s3, v6
	v_ashrrev_i32_e32 v7, 31, v6
	v_lshl_add_u64 v[6:7], v[6:7], 2, s[30:31]
	global_load_dword v244, v[6:7], off
	v_mov_b32_e32 v208, s3
	v_lshl_or_b32 v2, s2, 3, v222
	v_ashrrev_i32_e32 v3, 31, v2
	v_lshlrev_b64 v[2:3], 13, v[2:3]
	s_waitcnt lgkmcnt(0)
	v_lshl_add_u64 v[6:7], s[4:5], 0, v[2:3]
	v_mov_b32_e32 v2, 0
	v_lshlrev_b32_e32 v206, 4, v1
	v_mov_b32_e32 v207, v2
	v_lshl_add_u64 v[6:7], v[6:7], 0, v[206:207]
	v_lshlrev_b32_e32 v211, 13, v222
	v_ashrrev_i32_e32 v209, 31, v208
	v_lshl_add_u64 v[8:9], v[208:209], 2, s[30:31]
	v_or_b32_e32 v3, v211, v206
	v_lshl_add_u64 v[8:9], v[8:9], 0, v[206:207]
	global_load_dwordx4 v[68:71], v[8:9], off
	global_load_dwordx4 v[130:133], v[6:7], off
	global_load_dwordx4 v[134:137], v[6:7], off offset:1024
	global_load_dwordx4 v[138:141], v[6:7], off offset:2048
	global_load_dwordx4 v[142:145], v[6:7], off offset:3072
	s_movk_i32 s33, 0x1000
	v_add_co_u32_e32 v14, vcc, s33, v6
	s_nop 1
	v_addc_co_u32_e32 v15, vcc, 0, v7, vcc
	global_load_dwordx4 v[146:149], v[14:15], off
	global_load_dwordx4 v[150:153], v[14:15], off offset:1024
	global_load_dwordx4 v[154:157], v[14:15], off offset:2048
	global_load_dwordx4 v[158:161], v[14:15], off offset:3072
	v_lshlrev_b32_e32 v10, 1, v3
	global_load_dwordx4 v[186:189], v10, s[28:29] offset:16
	global_load_dwordx4 v[190:193], v10, s[28:29]
	global_load_dwordx4 v[178:181], v10, s[28:29] offset:2064
	global_load_dwordx4 v[182:185], v10, s[28:29] offset:2048
	v_mov_b32_e32 v11, v2
	v_lshl_add_u64 v[8:9], s[28:29], 0, v[10:11]
	v_add_co_u32_e32 v12, vcc, s33, v8
	s_mov_b64 s[34:35], 0x1000
	s_nop 0
	v_addc_co_u32_e32 v13, vcc, 0, v9, vcc
	s_mov_b64 s[40:41], 0x1800
	v_lshl_add_u64 v[10:11], v[8:9], 0, s[34:35]
	v_lshl_add_u64 v[8:9], v[8:9], 0, s[40:41]
	global_load_dwordx4 v[170:173], v[12:13], off
	global_load_dwordx4 v[174:177], v[10:11], off offset:16
	global_load_dwordx4 v[162:165], v[12:13], off offset:2048
	global_load_dwordx4 v[166:169], v[8:9], off offset:16
	s_waitcnt vmcnt(17)
	v_cmp_gt_u32_e32 vcc, 0x100, v0
	s_and_saveexec_b64 s[4:5], vcc
	v_lshlrev_b32_e32 v12, 4, v0
	v_and_b32_e32 v13, 0xe3, v0
	v_lshlrev_b32_e32 v14, 1, v0
	v_and_b32_e32 v12, 64, v12
	s_mov_b32 s8, 0x20000
	v_and_b32_e32 v14, 48, v14
	v_lshl_or_b32 v13, v13, 2, v12
	v_or3_b32 v13, v13, v14, s8
	v_add_f32_e32 v12, -1.0, v244
	v_mul_f32_e32 v12, 0x47000000, v12
	v_mul_f32_e32 v12, 0x3fb8aa3b, v12
	ds_write_b32 v13, v12
	s_or_b64 exec, exec, s[4:5]
	s_waitcnt lgkmcnt(0)
	s_barrier
	ds_read_b128 v[4:7], v206 offset:8192
	ds_read_b128 v[72:75], v206 offset:9216
	s_load_dwordx2 s[30:31], s[0:1], 0x38
	s_mov_b32 s0, 0x47000000
	s_mov_b32 s42, 0x3fb8aa3b
	s_mov_b32 s43, 0xff800000
	v_lshrrev_b32_e32 v96, 5, v1
	v_lshlrev_b32_e32 v97, 4, v96
	v_lshl_or_b32 v209, v222, 11, v206
	v_lshlrev_b32_e32 v1, 5, v1
	s_add_u32 s54, s24, 0x8000
	v_lshlrev_b32_e32 v207, 2, v96
	s_addc_u32 s55, s25, 0
	v_or_b32_e32 v227, 0x10000, v3
	s_mov_b32 s56, 0xc1d00000
	s_mov_b64 s[44:45], 0x20000
	s_mov_b64 s[46:47], 0x20800
	s_mov_b64 s[48:49], 0x21000
	s_mov_b32 s57, 0x21000
	s_mov_b64 s[50:51], 0x21800
	v_mov_b32_e32 v194, 0x3c003c00
	s_waitcnt lgkmcnt(0)
	s_waitcnt vmcnt(15)
	v_mfma_f32_32x32x16_f16 v[36:51], v[4:7], v[130:133], 0
	ds_read_b128 v[4:7], v206
	ds_read_b128 v[76:79], v206 offset:1024
	ds_read_b128 v[20:23], v206 offset:24576
	ds_read_b128 v[80:83], v206 offset:25600
	ds_read_b128 v[52:55], v206 offset:16384
	ds_read_b128 v[84:87], v206 offset:17408
	v_max_f32_e32 v71, v71, v71
	s_waitcnt lgkmcnt(1)
	v_mfma_f32_32x32x16_f16 v[52:67], v[130:133], v[52:55], 0
	v_max_f32_e32 v70, v70, v70
	v_max_f32_e32 v70, v70, v71
	s_waitcnt vmcnt(14)
	v_mfma_f32_32x32x16_f16 v[36:51], v[72:75], v[134:137], v[36:51]
	s_waitcnt lgkmcnt(0)
	v_mfma_f32_32x32x16_f16 v[52:67], v[134:137], v[84:87], v[52:67]
	ds_read_b128 v[72:75], v206 offset:10240
	ds_read_b128 v[84:87], v206 offset:11264
	s_waitcnt lgkmcnt(1)
	s_waitcnt vmcnt(13)
	v_mfma_f32_32x32x16_f16 v[36:51], v[72:75], v[138:141], v[36:51]
	ds_read_b128 v[72:75], v206 offset:18432
	ds_read_b128 v[88:91], v206 offset:19456
	s_waitcnt lgkmcnt(1)
	v_mfma_f32_32x32x16_f16 v[52:67], v[138:141], v[72:75], v[52:67]
	ds_read_b128 v[72:75], v206 offset:12288
	s_waitcnt vmcnt(12)
	v_mfma_f32_32x32x16_f16 v[36:51], v[84:87], v[142:145], v[36:51]
	v_mbcnt_lo_u32_b32 v84, -1, 0
	v_mbcnt_hi_u32_b32 v92, -1, v84
	ds_read_b128 v[84:87], v206 offset:13312
	v_xor_b32_e32 v93, 1, v92
	v_xor_b32_e32 v94, 2, v92
	v_xor_b32_e32 v95, 4, v92
	s_waitcnt lgkmcnt(2)
	v_mfma_f32_32x32x16_f16 v[52:67], v[142:145], v[88:91], v[52:67]
	v_and_b32_e32 v88, 64, v92
	v_add_u32_e32 v98, 64, v88
	v_cmp_lt_i32_e32 vcc, v93, v98
	ds_read_b128 v[88:91], v206 offset:21504
	s_waitcnt lgkmcnt(2)
	s_waitcnt vmcnt(11)
	v_mfma_f32_32x32x16_f16 v[36:51], v[72:75], v[146:149], v[36:51]
	ds_read_b128 v[72:75], v206 offset:20480
	s_waitcnt lgkmcnt(0)
	v_mfma_f32_32x32x16_f16 v[52:67], v[146:149], v[72:75], v[52:67]
	v_cndmask_b32_e32 v72, v92, v93, vcc
	v_lshlrev_b32_e32 v72, 2, v72
	v_max3_f32 v73, v68, v69, v70
	ds_bpermute_b32 v72, v72, v73
	v_cmp_lt_i32_e32 vcc, v94, v98
	s_waitcnt lgkmcnt(0)
	v_max_f32_e32 v72, v72, v72
	v_cndmask_b32_e32 v68, v92, v94, vcc
	v_lshlrev_b32_e32 v74, 2, v68
	ds_read_b128 v[68:71], v206 offset:14336
	s_waitcnt vmcnt(10)
	v_mfma_f32_32x32x16_f16 v[36:51], v[84:87], v[150:153], v[36:51]
	v_max_f32_e32 v84, v73, v72
	ds_bpermute_b32 v85, v74, v84
	v_cmp_lt_i32_e32 vcc, v95, v98
	s_waitcnt lgkmcnt(0)
	v_max_f32_e32 v85, v85, v85
	v_mfma_f32_32x32x16_f16 v[52:67], v[150:153], v[88:91], v[52:67]
	v_cndmask_b32_e32 v72, v92, v95, vcc
	v_lshlrev_b32_e32 v86, 2, v72
	v_max_f32_e32 v92, v84, v85
	ds_read_b128 v[72:75], v206 offset:15360
	ds_bpermute_b32 v93, v86, v92
	s_waitcnt lgkmcnt(0)
	v_max_f32_e32 v93, v93, v93
	s_waitcnt vmcnt(9)
	v_mfma_f32_32x32x16_f16 v[36:51], v[68:71], v[154:157], v[36:51]
	ds_read_b128 v[68:71], v206 offset:22528
	ds_read_b128 v[84:87], v206 offset:23552
	v_max_f32_e32 v92, v92, v93
	global_load_dwordx4 v[88:91], v97, s[36:37]
	v_readlane_b32 s3, v92, 0
	v_readlane_b32 s2, v92, 8
	v_readlane_b32 s5, v92, 16
	v_readlane_b32 s4, v92, 24
	s_waitcnt lgkmcnt(1)
	v_mfma_f32_32x32x16_f16 v[52:67], v[154:157], v[68:71], v[52:67]
	v_add_f32_e64 v68, s2, -1.0
	v_add_f32_e64 v69, s3, -1.0
	v_readlane_b32 s7, v92, 32
	v_readlane_b32 s6, v92, 40
	v_add_f32_e64 v70, s4, -1.0
	v_add_f32_e64 v71, s5, -1.0
	v_pk_mul_f32 v[68:69], v[68:69], s[0:1] op_sel_hi:[1,0]
	v_readlane_b32 s9, v92, 48
	v_readlane_b32 s8, v92, 56
	v_mfma_f32_32x32x16_f16 v[20:35], v[20:23], v[130:133], 0
	v_mul_f32_e64 v70, v70, s0
	v_mul_f32_e64 v71, v71, s0
	v_mul_f32_e64 v92, v68, s42
	v_mul_f32_e64 v93, v69, s42
	v_mul_f32_e64 v94, v70, s42
	v_mul_f32_e64 v95, v71, s42
	v_max3_f32 v68, v93, s43, v92
	v_max3_f32 v68, v68, v95, v94
	s_waitcnt vmcnt(9)
	v_mfma_f32_32x32x16_f16 v[36:51], v[72:75], v[158:161], v[36:51]
	v_add_f32_e64 v72, s6, -1.0
	v_add_f32_e64 v73, s7, -1.0
	v_mul_f32_e64 v72, v72, s0
	v_mul_f32_e64 v73, v73, s0
	s_waitcnt lgkmcnt(0)
	v_mfma_f32_32x32x16_f16 v[52:67], v[158:161], v[84:87], v[52:67]
	v_mul_f32_e64 v84, v72, s42
	v_mul_f32_e64 v85, v73, s42
	v_add_f32_e64 v86, s8, -1.0
	v_add_f32_e64 v87, s9, -1.0
	v_max3_f32 v98, v68, v85, v84
	ds_read_b128 v[68:71], v206 offset:26624
	v_cvt_pk_f16_f32 v43, v42, v43
	v_cvt_pk_f16_f32 v42, v40, v41
	v_cvt_pk_f16_f32 v41, v38, v39
	v_mfma_f32_32x32x16_f16 v[20:35], v[80:83], v[134:137], v[20:35]
	v_mul_f32_e64 v80, v86, s0
	v_mul_f32_e64 v81, v87, s0
	v_cvt_pk_f16_f32 v40, v36, v37
	v_mul_f32_e64 v86, v80, s42
	v_mul_f32_e64 v87, v81, s42
	global_load_dwordx4 v[72:75], v97, s[36:37] offset:32
	v_max3_f32 v80, v98, v87, v86
	v_add_f32_e32 v98, 0xc53b8000, v80
	ds_read_b128 v[80:83], v206 offset:27648
	global_load_dwordx4 v[36:39], v97, s[36:37] offset:64
	ds_write_b128 v209, v[40:43] offset:32768
	v_cvt_pk_f16_f32 v43, v50, v51
	v_cvt_pk_f16_f32 v40, v44, v45
	v_cvt_pk_f16_f32 v44, v52, v53
	global_load_dwordx4 v[50:53], v97, s[36:37] offset:96
	s_waitcnt lgkmcnt(2)
	v_mfma_f32_32x32x16_f16 v[20:35], v[68:71], v[138:141], v[20:35]
	ds_read_b128 v[68:71], v206 offset:28672
	v_cvt_pk_f16_f32 v42, v48, v49
	v_cvt_pk_f16_f32 v41, v46, v47
	ds_write_b128 v209, v[40:43] offset:33792
	ds_read_b128 v[40:43], v206 offset:30720
	v_cvt_pk_f16_f32 v47, v58, v59
	v_cvt_pk_f16_f32 v46, v56, v57
	s_waitcnt lgkmcnt(4)
	v_mfma_f32_32x32x16_f16 v[20:35], v[80:83], v[142:145], v[20:35]
	ds_read_b128 v[80:83], v206 offset:29696
	v_cvt_pk_f16_f32 v45, v54, v55
	ds_write_b128 v209, v[44:47] offset:49152
	v_cvt_pk_f16_f32 v45, v66, v67
	ds_read_b128 v[46:49], v206 offset:31744
	v_cvt_pk_f16_f32 v44, v64, v65
	v_cmp_ge_f32_e64 s[0:1], v92, v98
	s_waitcnt lgkmcnt(5)
	v_mfma_f32_32x32x16_f16 v[20:35], v[68:71], v[146:149], v[20:35]
	v_cmp_ge_f32_e64 s[2:3], v93, v98
	v_cmp_ge_f32_e64 s[4:5], v94, v98
	v_cmp_ge_f32_e64 s[6:7], v95, v98
	v_cmp_ge_f32_e64 s[8:9], v84, v98
	v_cmp_ge_f32_e64 s[10:11], v85, v98
	v_cmp_ge_f32_e64 s[12:13], v86, v98
	v_cmp_ge_f32_e64 s[14:15], v87, v98
	v_mfma_f32_32x32x16_f16 v[4:19], v[4:7], v[130:133], 0
	s_waitcnt lgkmcnt(2)
	v_mfma_f32_32x32x16_f16 v[20:35], v[80:83], v[150:153], v[20:35]
	v_mfma_f32_32x32x16_f16 v[4:19], v[76:79], v[134:137], v[4:19]
	v_mfma_f32_32x32x16_f16 v[20:35], v[40:43], v[154:157], v[20:35]
	v_cvt_pk_f16_f32 v43, v62, v63
	v_cvt_pk_f16_f32 v42, v60, v61
	ds_write_b128 v209, v[42:45] offset:50176
	ds_read_b128 v[40:43], v206 offset:2048
	ds_read_b128 v[54:57], v206 offset:3072
	s_waitcnt lgkmcnt(1)
	v_mfma_f32_32x32x16_f16 v[4:19], v[40:43], v[138:141], v[4:19]
	s_waitcnt lgkmcnt(0)
	v_mfma_f32_32x32x16_f16 v[4:19], v[54:57], v[142:145], v[4:19]
	v_mfma_f32_32x32x16_f16 v[20:35], v[46:49], v[158:161], v[20:35]
	ds_read_b128 v[44:47], v206 offset:4096
	ds_read_b128 v[58:61], v206 offset:5120
	ds_read_b128 v[62:65], v206 offset:6144
	ds_read_b128 v[66:69], v206 offset:7168
	s_waitcnt lgkmcnt(0)
	s_barrier
	s_waitcnt vmcnt(3)
	s_nop 4
	v_add_f32_e32 v20, v20, v88
	v_mfma_f32_32x32x16_f16 v[4:19], v[44:47], v[146:149], v[4:19]
	v_add_f32_e32 v21, v89, v21
	v_add_f32_e32 v22, v90, v22
	v_add_f32_e32 v23, v91, v23
	s_waitcnt vmcnt(2)
	v_add_f32_e32 v24, v24, v72
	v_add_f32_e32 v25, v73, v25
	v_add_f32_e32 v26, v74, v26
	v_add_f32_e32 v27, v75, v27
	v_mfma_f32_32x32x16_f16 v[4:19], v[58:61], v[150:153], v[4:19]
	s_waitcnt vmcnt(1)
	v_add_f32_e32 v28, v28, v36
	v_add_f32_e32 v29, v37, v29
	v_add_f32_e32 v30, v38, v30
	v_add_f32_e32 v31, v39, v31
	s_waitcnt vmcnt(0)
	v_add_f32_e32 v32, v32, v50
	v_add_f32_e32 v33, v51, v33
	v_add_f32_e32 v34, v52, v34
	v_mfma_f32_32x32x16_f16 v[4:19], v[62:65], v[154:157], v[4:19]
	v_add_f32_e32 v35, v53, v35
	v_mul_f32_e32 v20, 0xbfb8aa3b, v20
	v_mul_f32_e32 v21, 0xbfb8aa3b, v21
	v_mul_f32_e32 v22, 0xbfb8aa3b, v22
	v_mul_f32_e32 v23, 0xbfb8aa3b, v23
	v_mul_f32_e32 v24, 0xbfb8aa3b, v24
	v_mul_f32_e32 v25, 0xbfb8aa3b, v25
	v_mfma_f32_32x32x16_f16 v[4:19], v[66:69], v[158:161], v[4:19]
	v_mul_f32_e32 v26, 0xbfb8aa3b, v26
	v_mul_f32_e32 v27, 0xbfb8aa3b, v27
	v_mul_f32_e32 v28, 0xbfb8aa3b, v28
	v_mul_f32_e32 v29, 0xbfb8aa3b, v29
	v_mul_f32_e32 v30, 0xbfb8aa3b, v30
	v_mul_f32_e32 v31, 0xbfb8aa3b, v31
	v_mul_f32_e32 v32, 0xbfb8aa3b, v32
	v_mul_f32_e32 v33, 0xbfb8aa3b, v33
	v_mul_f32_e32 v34, 0xbfb8aa3b, v34
	v_mul_f32_e32 v35, 0xbfb8aa3b, v35
	v_exp_f32_e32 v20, v20
	v_exp_f32_e32 v21, v21
	v_exp_f32_e32 v22, v22
	v_exp_f32_e32 v23, v23
	v_exp_f32_e32 v24, v24
	v_exp_f32_e32 v25, v25
	v_exp_f32_e32 v26, v26
	v_exp_f32_e32 v27, v27
	v_exp_f32_e32 v28, v28
	v_exp_f32_e32 v29, v29
	v_exp_f32_e32 v30, v30
	v_exp_f32_e32 v31, v31
	v_exp_f32_e32 v32, v32
	v_exp_f32_e32 v33, v33
	v_exp_f32_e32 v34, v34
	v_exp_f32_e32 v35, v35
	v_add_f32_e32 v20, 1.0, v20
	v_add_f32_e32 v21, 1.0, v21
	v_add_f32_e32 v22, 1.0, v22
	v_add_f32_e32 v23, 1.0, v23
	v_add_f32_e32 v24, 1.0, v24
	v_add_f32_e32 v25, 1.0, v25
	v_add_f32_e32 v26, 1.0, v26
	v_add_f32_e32 v27, 1.0, v27
	v_add_f32_e32 v28, 1.0, v28
	v_add_f32_e32 v29, 1.0, v29
	v_add_f32_e32 v30, 1.0, v30
	v_add_f32_e32 v31, 1.0, v31
	v_add_f32_e32 v32, 1.0, v32
	v_add_f32_e32 v33, 1.0, v33
	v_add_f32_e32 v34, 1.0, v34
	v_add_f32_e32 v35, 1.0, v35
	v_rcp_f32_e32 v20, v20
	v_rcp_f32_e32 v21, v21
	v_rcp_f32_e32 v22, v22
	v_rcp_f32_e32 v23, v23
	v_rcp_f32_e32 v24, v24
	v_rcp_f32_e32 v25, v25
	v_rcp_f32_e32 v26, v26
	v_rcp_f32_e32 v27, v27
	v_rcp_f32_e32 v28, v28
	v_rcp_f32_e32 v29, v29
	v_rcp_f32_e32 v30, v30
	v_rcp_f32_e32 v31, v31
	v_rcp_f32_e32 v32, v32
	v_rcp_f32_e32 v33, v33
	v_rcp_f32_e32 v34, v34
	v_rcp_f32_e32 v35, v35
	v_cvt_pk_f16_f32 v198, v4, v5
	v_lshl_or_b32 v4, v222, 14, v1
	v_mov_b32_e32 v5, v2
	v_lshl_add_u64 v[216:217], s[28:29], 0, v[4:5]
	v_or_b32_e32 v4, 0x2000, v4
	v_lshrrev_b32_e32 v1, 1, v0
	v_lshl_add_u64 v[218:219], s[28:29], 0, v[4:5]
	v_and_b32_e32 v4, 16, v1
	v_mov_b32_e32 v36, 0x20000
	v_lshl_add_u64 v[4:5], s[36:37], 0, v[4:5]
	s_mov_b64 s[28:29], 0x80
	v_lshl_or_b32 v226, v96, 6, v36
	v_cvt_pk_f16_f32 v199, v6, v7
	v_cvt_pk_f16_f32 v200, v8, v9
	v_cvt_pk_f16_f32 v201, v10, v11
	v_cvt_pk_f16_f32 v202, v12, v13
	v_cvt_pk_f16_f32 v203, v14, v15
	v_cvt_pk_f16_f32 v204, v16, v17
	v_cvt_pk_f16_f32 v205, v18, v19
	v_cvt_pk_f16_f32 v229, v20, v21
	v_cvt_pk_f16_f32 v230, v22, v23
	v_cvt_pk_f16_f32 v232, v24, v25
	v_cvt_pk_f16_f32 v234, v26, v27
	v_cvt_pk_f16_f32 v228, v28, v29
	v_cvt_pk_f16_f32 v231, v30, v31
	v_cvt_pk_f16_f32 v233, v32, v33
	v_cvt_pk_f16_f32 v235, v34, v35
	v_lshl_add_u64 v[220:221], v[4:5], 0, s[28:29]
	s_mov_b64 s[36:37], 0
	v_readfirstlane_b32 s63, v222
	s_mov_b32 s70, 0
	s_cmp_lg_u64 s[2:3], 0
	s_cselect_b32 s71, 1, 0
	s_or_b32 s70, s70, s71
	s_cmp_lg_u64 s[0:1], 0
	s_cselect_b32 s71, 2, 0
	s_or_b32 s70, s70, s71
	s_cmp_lg_u64 s[6:7], 0
	s_cselect_b32 s71, 4, 0
	s_or_b32 s70, s70, s71
	s_cmp_lg_u64 s[4:5], 0
	s_cselect_b32 s71, 8, 0
	s_or_b32 s70, s70, s71
	s_cmp_lg_u64 s[10:11], 0
	s_cselect_b32 s71, 16, 0
	s_or_b32 s70, s70, s71
	s_cmp_lg_u64 s[8:9], 0
	s_cselect_b32 s71, 32, 0
	s_or_b32 s70, s70, s71
	s_cmp_lg_u64 s[14:15], 0
	s_cselect_b32 s71, 64, 0
	s_or_b32 s70, s70, s71
	s_cmp_lg_u64 s[12:13], 0
	s_cselect_b32 s71, 0x80, 0
	s_or_b32 s70, s70, s71
	s_lshr_b32 s70, s70, s63
	s_and_b32 s70, s70, 1
	s_branch .LBB1_6

.LBB1_59:
	s_setprio 0
	s_nop 10
	v_rcp_f32_e32 v8, v82
	v_cvt_f32_f16_sdwa v5, v229 dst_sel:DWORD dst_unused:UNUSED_PAD src0_sel:WORD_1
	v_cvt_f32_f16_e32 v4, v229
	v_cvt_f32_f16_sdwa v7, v230 dst_sel:DWORD dst_unused:UNUSED_PAD src0_sel:WORD_1
	v_cvt_f32_f16_e32 v6, v230
	v_cvt_f32_f16_sdwa v11, v232 dst_sel:DWORD dst_unused:UNUSED_PAD src0_sel:WORD_1
	v_cvt_f32_f16_e32 v10, v232
	v_cvt_f32_f16_sdwa v13, v234 dst_sel:DWORD dst_unused:UNUSED_PAD src0_sel:WORD_1
	v_cvt_f32_f16_e32 v12, v234
	v_pk_mul_f32 v[4:5], v[8:9], v[4:5] op_sel_hi:[0,1]
	v_pk_mul_f32 v[6:7], v[8:9], v[6:7] op_sel_hi:[0,1]
	v_pk_mul_f32 v[4:5], v[98:99], v[4:5]
	v_pk_mul_f32 v[6:7], v[100:101], v[6:7]
	v_cvt_pk_f16_f32 v4, v4, v5
	v_cvt_pk_f16_f32 v5, v6, v7
	v_pk_mul_f32 v[6:7], v[8:9], v[10:11] op_sel_hi:[0,1]
	v_pk_mul_f32 v[10:11], v[8:9], v[12:13] op_sel_hi:[0,1]
	v_pk_mul_f32 v[6:7], v[102:103], v[6:7]
	v_pk_mul_f32 v[10:11], v[104:105], v[10:11]
	v_cvt_pk_f16_f32 v6, v6, v7
	v_cvt_pk_f16_f32 v7, v10, v11
	v_cvt_f32_f16_sdwa v11, v228 dst_sel:DWORD dst_unused:UNUSED_PAD src0_sel:WORD_1
	v_cvt_f32_f16_e32 v10, v228
	ds_write_b128 v227, v[4:7]
	v_cvt_f32_f16_sdwa v7, v231 dst_sel:DWORD dst_unused:UNUSED_PAD src0_sel:WORD_1
	v_cvt_f32_f16_e32 v6, v231
	v_pk_mul_f32 v[4:5], v[8:9], v[10:11] op_sel_hi:[0,1]
	v_cvt_f32_f16_sdwa v11, v233 dst_sel:DWORD dst_unused:UNUSED_PAD src0_sel:WORD_1
	v_cvt_f32_f16_e32 v10, v233
	v_cvt_f32_f16_sdwa v13, v235 dst_sel:DWORD dst_unused:UNUSED_PAD src0_sel:WORD_1
	v_cvt_f32_f16_e32 v12, v235
	v_pk_mul_f32 v[6:7], v[8:9], v[6:7] op_sel_hi:[0,1]
	v_pk_mul_f32 v[4:5], v[4:5], v[106:107]
	v_pk_mul_f32 v[6:7], v[6:7], v[108:109]
	v_cvt_pk_f16_f32 v4, v4, v5
	v_cvt_pk_f16_f32 v5, v6, v7
	v_pk_mul_f32 v[6:7], v[8:9], v[10:11] op_sel_hi:[0,1]
	v_pk_mul_f32 v[8:9], v[8:9], v[12:13] op_sel_hi:[0,1]
	v_pk_mul_f32 v[6:7], v[6:7], v[110:111]
	v_pk_mul_f32 v[8:9], v[8:9], v[112:113]
	v_cvt_pk_f16_f32 v6, v6, v7
	v_cvt_pk_f16_f32 v7, v8, v9
	s_and_b64 vcc, exec, s[16:17]
	ds_write_b128 v227, v[4:7] offset:1024
	s_waitcnt vmcnt(0) lgkmcnt(0)
	s_barrier
	s_cbranch_vccnz .LBB1_5
	s_cmp_eq_u32 s70, 0
	s_cbranch_scc1 .Lproj_dead
	ds_read_b128 v[4:7], v206 offset:8192
	ds_read_b128 v[8:11], v206 offset:9216
	s_waitcnt lgkmcnt(1)
	v_mfma_f32_32x32x16_f16 v[114:129], v[4:7], v[130:133], 0
	ds_read_b128 v[4:7], v206 offset:16384
	ds_read_b128 v[12:15], v206 offset:17408
	s_waitcnt lgkmcnt(1)
	v_mfma_f32_32x32x16_f16 v[98:113], v[130:133], v[4:7], 0
	v_mfma_f32_32x32x16_f16 v[114:129], v[8:11], v[134:137], v[114:129]
	ds_read_b128 v[4:7], v206 offset:10240
	ds_read_b128 v[8:11], v206 offset:11264
	s_waitcnt lgkmcnt(2)
	v_mfma_f32_32x32x16_f16 v[98:113], v[134:137], v[12:15], v[98:113]
	s_waitcnt lgkmcnt(1)
	v_mfma_f32_32x32x16_f16 v[114:129], v[4:7], v[138:141], v[114:129]
	ds_read_b128 v[4:7], v206 offset:18432
	ds_read_b128 v[12:15], v206 offset:19456
	s_waitcnt lgkmcnt(1)
	v_mfma_f32_32x32x16_f16 v[98:113], v[138:141], v[4:7], v[98:113]
	v_mfma_f32_32x32x16_f16 v[114:129], v[8:11], v[142:145], v[114:129]
	ds_read_b128 v[4:7], v206 offset:12288
	ds_read_b128 v[8:11], v206 offset:13312
	s_waitcnt lgkmcnt(2)
	v_mfma_f32_32x32x16_f16 v[98:113], v[142:145], v[12:15], v[98:113]
	s_waitcnt lgkmcnt(1)
	v_mfma_f32_32x32x16_f16 v[114:129], v[4:7], v[146:149], v[114:129]
	ds_read_b128 v[4:7], v206 offset:20480
	ds_read_b128 v[12:15], v206 offset:21504
	s_waitcnt lgkmcnt(1)
	v_mfma_f32_32x32x16_f16 v[98:113], v[146:149], v[4:7], v[98:113]
	v_mfma_f32_32x32x16_f16 v[114:129], v[8:11], v[150:153], v[114:129]
	ds_read_b128 v[4:7], v206 offset:14336
	ds_read_b128 v[8:11], v206 offset:15360
	s_waitcnt lgkmcnt(2)
	v_mfma_f32_32x32x16_f16 v[98:113], v[150:153], v[12:15], v[98:113]
	s_waitcnt lgkmcnt(1)
	v_mfma_f32_32x32x16_f16 v[114:129], v[4:7], v[154:157], v[114:129]
	ds_read_b128 v[4:7], v206 offset:22528
	ds_read_b128 v[12:15], v206 offset:23552
	s_waitcnt lgkmcnt(1)
	v_mfma_f32_32x32x16_f16 v[98:113], v[154:157], v[4:7], v[98:113]
	v_mfma_f32_32x32x16_f16 v[114:129], v[8:11], v[158:161], v[114:129]
	ds_read_b128 v[4:7], v206 offset:24576
	ds_read_b128 v[8:11], v206 offset:25600
	s_waitcnt lgkmcnt(1)
	v_mfma_f32_32x32x16_f16 v[82:97], v[4:7], v[130:133], 0
	global_load_dwordx4 v[4:7], v[220:221], off
	s_nop 6
	v_cvt_pk_f16_f32 v121, v120, v121
	v_cvt_pk_f16_f32 v120, v118, v119
	v_cvt_pk_f16_f32 v119, v116, v117
	v_cvt_pk_f16_f32 v118, v114, v115
	v_cvt_pk_f16_f32 v117, v128, v129
	v_cvt_pk_f16_f32 v116, v126, v127
	s_waitcnt lgkmcnt(0)
	v_mfma_f32_32x32x16_f16 v[82:97], v[8:11], v[134:137], v[82:97]
	v_cvt_pk_f16_f32 v115, v124, v125
	v_cvt_pk_f16_f32 v114, v122, v123
	v_mfma_f32_32x32x16_f16 v[98:113], v[158:161], v[12:15], v[98:113]
	ds_read_b128 v[8:11], v206 offset:26624
	ds_read_b128 v[12:15], v206 offset:27648
	ds_read_b128 v[196:199], v206 offset:28672
	ds_write_b128 v209, v[114:117] offset:33792
	global_load_dwordx4 v[114:117], v[220:221], off offset:96
	ds_write_b128 v209, v[118:121] offset:32768
	ds_read_b128 v[118:121], v206 offset:29696
	s_nop 4
	v_cvt_pk_f16_f32 v105, v104, v105
	s_waitcnt lgkmcnt(5)
	v_mfma_f32_32x32x16_f16 v[82:97], v[8:11], v[138:141], v[82:97]
	global_load_dwordx4 v[8:11], v[220:221], off offset:32
	v_cvt_pk_f16_f32 v104, v102, v103
	v_cvt_pk_f16_f32 v103, v100, v101
	v_cvt_pk_f16_f32 v102, v98, v99
	ds_read_b128 v[98:101], v206 offset:30720
	ds_write_b128 v209, v[102:105] offset:49152
	v_cvt_pk_f16_f32 v103, v108, v109
	s_waitcnt lgkmcnt(6)
	v_mfma_f32_32x32x16_f16 v[82:97], v[12:15], v[142:145], v[82:97]
	global_load_dwordx4 v[12:15], v[220:221], off offset:64
	v_cvt_pk_f16_f32 v102, v106, v107
	ds_read_b128 v[106:109], v206 offset:31744
	v_cvt_pk_f16_f32 v105, v112, v113
	v_cvt_pk_f16_f32 v104, v110, v111
	ds_write_b128 v209, v[102:105] offset:50176
	s_waitcnt lgkmcnt(7)
	v_mfma_f32_32x32x16_f16 v[82:97], v[196:199], v[146:149], v[82:97]
	s_waitcnt lgkmcnt(4)
	v_mfma_f32_32x32x16_f16 v[82:97], v[118:121], v[150:153], v[82:97]
	s_waitcnt lgkmcnt(3)
	v_mfma_f32_32x32x16_f16 v[82:97], v[98:101], v[154:157], v[82:97]
	ds_read_b128 v[98:101], v206
	ds_read_b128 v[118:121], v206 offset:1024
	ds_read_b128 v[122:125], v206 offset:2048
	ds_read_b128 v[126:129], v206 offset:3072
	ds_read_b128 v[196:199], v206 offset:4096
	ds_read_b128 v[200:203], v206 offset:5120
	ds_read_b128 v[230:233], v206 offset:6144
	ds_read_b128 v[236:239], v206 offset:7168
	s_waitcnt lgkmcnt(0)
.Lproj_join:
	s_barrier
	v_mfma_f32_32x32x16_f16 v[82:97], v[106:109], v[158:161], v[82:97]
	v_mfma_f32_32x32x16_f16 v[98:113], v[98:101], v[130:133], 0
	s_waitcnt vmcnt(3)
	s_nop 9
	v_add_f32_e32 v1, v82, v4
	v_mfma_f32_32x32x16_f16 v[98:113], v[118:121], v[134:137], v[98:113]
	v_add_f32_e32 v3, v5, v83
	v_add_f32_e32 v4, v6, v84
	v_add_f32_e32 v5, v7, v85
	v_mul_f32_e32 v1, 0xbfb8aa3b, v1
	v_mul_f32_e32 v3, 0xbfb8aa3b, v3
	v_mul_f32_e32 v4, 0xbfb8aa3b, v4
	v_mul_f32_e32 v5, 0xbfb8aa3b, v5
	v_mfma_f32_32x32x16_f16 v[98:113], v[122:125], v[138:141], v[98:113]
	v_exp_f32_e32 v1, v1
	v_exp_f32_e32 v3, v3
	v_exp_f32_e32 v4, v4
	v_exp_f32_e32 v5, v5
	v_add_f32_e32 v1, 1.0, v1
	v_add_f32_e32 v3, 1.0, v3
	v_add_f32_e32 v4, 1.0, v4
	v_mfma_f32_32x32x16_f16 v[98:113], v[126:129], v[142:145], v[98:113]
	v_add_f32_e32 v5, 1.0, v5
	s_waitcnt vmcnt(2)
	v_add_f32_e32 v16, v116, v96
	v_add_f32_e32 v17, v117, v97
	v_mul_f32_e32 v16, 0xbfb8aa3b, v16
	v_mul_f32_e32 v17, 0xbfb8aa3b, v17
	v_exp_f32_e32 v16, v16
	v_exp_f32_e32 v17, v17
	v_mfma_f32_32x32x16_f16 v[98:113], v[196:199], v[146:149], v[98:113]
	s_waitcnt vmcnt(1)
	v_add_f32_e32 v6, v86, v8
	v_add_f32_e32 v7, v9, v87
	v_add_f32_e32 v8, v10, v88
	v_add_f32_e32 v9, v11, v89
	v_mul_f32_e32 v6, 0xbfb8aa3b, v6
	v_mul_f32_e32 v7, 0xbfb8aa3b, v7
	v_mul_f32_e32 v8, 0xbfb8aa3b, v8
	v_mfma_f32_32x32x16_f16 v[98:113], v[200:203], v[150:153], v[98:113]
	s_waitcnt vmcnt(0)
	v_add_f32_e32 v10, v90, v12
	v_add_f32_e32 v11, v13, v91
	v_add_f32_e32 v12, v14, v92
	v_add_f32_e32 v13, v15, v93
	v_add_f32_e32 v14, v94, v114
	v_add_f32_e32 v15, v115, v95
	v_mul_f32_e32 v9, 0xbfb8aa3b, v9
	v_mfma_f32_32x32x16_f16 v[98:113], v[230:233], v[154:157], v[98:113]
	v_mul_f32_e32 v10, 0xbfb8aa3b, v10
	v_mul_f32_e32 v11, 0xbfb8aa3b, v11
	v_mul_f32_e32 v12, 0xbfb8aa3b, v12
	v_mul_f32_e32 v13, 0xbfb8aa3b, v13
	v_mul_f32_e32 v14, 0xbfb8aa3b, v14
	v_mul_f32_e32 v15, 0xbfb8aa3b, v15
	v_exp_f32_e32 v6, v6
	v_exp_f32_e32 v7, v7
	v_exp_f32_e32 v8, v8
	v_exp_f32_e32 v9, v9
	v_exp_f32_e32 v10, v10
	v_exp_f32_e32 v11, v11
	v_exp_f32_e32 v12, v12
	v_exp_f32_e32 v13, v13
	v_exp_f32_e32 v14, v14
	v_exp_f32_e32 v15, v15
	v_mfma_f32_32x32x16_f16 v[98:113], v[236:239], v[158:161], v[98:113]
	v_add_f32_e32 v6, 1.0, v6
	v_add_f32_e32 v7, 1.0, v7
	v_add_f32_e32 v8, 1.0, v8
	v_add_f32_e32 v9, 1.0, v9
	v_add_f32_e32 v10, 1.0, v10
	v_add_f32_e32 v11, 1.0, v11
	v_add_f32_e32 v12, 1.0, v12
	v_add_f32_e32 v13, 1.0, v13
	v_add_f32_e32 v14, 1.0, v14
	v_add_f32_e32 v15, 1.0, v15
	v_add_f32_e32 v16, 1.0, v16
	v_add_f32_e32 v17, 1.0, v17
	v_rcp_f32_e32 v1, v1
	v_rcp_f32_e32 v3, v3
	v_rcp_f32_e32 v4, v4
	v_rcp_f32_e32 v5, v5
	v_rcp_f32_e32 v6, v6
	v_rcp_f32_e32 v7, v7
	v_rcp_f32_e32 v8, v8
	v_rcp_f32_e32 v9, v9
	v_rcp_f32_e32 v10, v10
	v_rcp_f32_e32 v11, v11
	v_rcp_f32_e32 v12, v12
	v_rcp_f32_e32 v13, v13
	v_rcp_f32_e32 v14, v14
	v_rcp_f32_e32 v15, v15
	v_rcp_f32_e32 v16, v16
	v_rcp_f32_e32 v17, v17
	v_cvt_pk_f16_f32 v228, v10, v11
	v_cvt_pk_f16_f32 v231, v12, v13
	v_cvt_pk_f16_f32 v233, v14, v15
	v_cvt_pk_f16_f32 v235, v16, v17
	v_cvt_pk_f16_f32 v229, v1, v3
	v_cvt_pk_f16_f32 v230, v4, v5
	v_cvt_pk_f16_f32 v232, v6, v7
	v_cvt_pk_f16_f32 v234, v8, v9
	v_cvt_pk_f16_f32 v202, v106, v107
	v_cvt_pk_f16_f32 v203, v108, v109
	v_cvt_pk_f16_f32 v204, v110, v111
	v_cvt_pk_f16_f32 v205, v112, v113
	v_cvt_pk_f16_f32 v198, v98, v99
	v_cvt_pk_f16_f32 v199, v100, v101
	v_cvt_pk_f16_f32 v200, v102, v103
	v_cvt_pk_f16_f32 v201, v104, v105
	s_branch .LBB1_5
.Lproj_dead:
	ds_read_b128 v[4:7], v206 offset:24576
	ds_read_b128 v[8:11], v206 offset:25600
	ds_read_b128 v[12:15], v206 offset:26624
	ds_read_b128 v[102:105], v206 offset:27648
	ds_read_b128 v[110:113], v206 offset:28672
	ds_read_b128 v[18:21], v206 offset:29696
	ds_read_b128 v[22:25], v206 offset:30720
	ds_read_b128 v[106:109], v206 offset:31744
	s_waitcnt lgkmcnt(7)
	v_mfma_f32_32x32x16_f16 v[82:97], v[4:7], v[130:133], 0
	global_load_dwordx4 v[4:7], v[220:221], off
	global_load_dwordx4 v[114:117], v[220:221], off offset:96
	s_waitcnt lgkmcnt(6)
	v_mfma_f32_32x32x16_f16 v[82:97], v[8:11], v[134:137], v[82:97]
	global_load_dwordx4 v[8:11], v[220:221], off offset:32
	s_waitcnt lgkmcnt(5)
	v_mfma_f32_32x32x16_f16 v[82:97], v[12:15], v[138:141], v[82:97]
	global_load_dwordx4 v[12:15], v[220:221], off offset:64
	ds_read_b128 v[98:101], v206
	ds_read_b128 v[118:121], v206 offset:1024
	ds_read_b128 v[122:125], v206 offset:2048
	ds_read_b128 v[126:129], v206 offset:3072
	s_waitcnt lgkmcnt(8)
	v_mfma_f32_32x32x16_f16 v[82:97], v[102:105], v[142:145], v[82:97]
	s_waitcnt lgkmcnt(7)
	v_mfma_f32_32x32x16_f16 v[82:97], v[110:113], v[146:149], v[82:97]
	ds_read_b128 v[196:199], v206 offset:4096
	ds_read_b128 v[200:203], v206 offset:5120
	ds_read_b128 v[230:233], v206 offset:6144
	ds_read_b128 v[236:239], v206 offset:7168
	s_waitcnt lgkmcnt(9)
	v_mfma_f32_32x32x16_f16 v[82:97], v[18:21], v[150:153], v[82:97]
	s_waitcnt lgkmcnt(8)
	v_mfma_f32_32x32x16_f16 v[82:97], v[22:25], v[154:157], v[82:97]
	s_waitcnt lgkmcnt(0)
	s_branch .Lproj_join
